# down-GEMM re-deal: blocks with a third gate|up unit take two down units (fallback to plain deal if more than half the blocks are late)
# speedup vs baseline: 1.0685x; 1.0049x over previous
.Lremap_g3_done:
	s_cmp_le_u32 s29, 128
	s_cbranch_scc1 .Lremap_ok
	s_mov_b32 s27, 0
	s_mov_b32 s28, 0
	s_mov_b32 s29, 0

.LBB0_1050:
	s_add_u32 s26, s26, 1
	s_cmp_lt_u32 s26, 2
	s_cbranch_scc0 .Lremap_extra
	s_addk_i32 s16, 0x100
	s_branch .Lremap_check
.Lremap_extra:
	s_cmp_eq_u32 s27, 1
	s_cbranch_scc1 .LBB0_1055
	s_cmp_eq_u32 s26, 2
	s_cbranch_scc0 .Lremap_next
	s_add_u32 s16, s28, 512
	s_branch .Lremap_check
